# v8 + P0 rotary table loop: the four position loads of an iteration issued as one batch (was load, vmcnt(0), convert per load)
# speedup vs baseline: 1.0077x; 1.0077x over previous
.LBB0_74:
	v_add_u32_e32 v6, s1, v19
	v_ashrrev_i32_e32 v8, 6, v6
	v_readlane_b32 s12, v252, 21
	v_ashrrev_i32_e32 v9, 31, v8
	v_readlane_b32 s16, v252, 25
	v_readlane_b32 s17, v252, 26
	v_readlane_b32 s14, v252, 23
	v_readlane_b32 s15, v252, 24
	v_lshl_add_u64 v[8:9], v[8:9], 2, s[16:17]
	global_load_dword v6, v[8:9], off
	v_mov_b32_e32 v232, 0
	v_mov_b32_e32 v233, 0
	v_mov_b32_e32 v234, 0
	v_add_u32_e32 v8, s40, v19
	v_cmp_gt_i32_e64 s[14:15], s38, v8
	v_mov_b32_e32 v12, 0
	v_readlane_b32 s13, v252, 22
	v_readlane_b32 s18, v252, 27
	v_readlane_b32 s19, v252, 28
	s_and_saveexec_b64 s[10:11], s[14:15]
	s_cbranch_execz .LBB0_76
	v_ashrrev_i32_e32 v8, 6, v8
	v_readlane_b32 s16, v252, 21
	v_ashrrev_i32_e32 v9, 31, v8
	v_readlane_b32 s20, v252, 25
	v_readlane_b32 s21, v252, 26
	v_readlane_b32 s17, v252, 22
	v_readlane_b32 s18, v252, 23
	v_lshl_add_u64 v[8:9], v[8:9], 2, s[20:21]
	global_load_dword v232, v[8:9], off
	v_readlane_b32 s19, v252, 24
	v_readlane_b32 s22, v252, 27
	v_readlane_b32 s23, v252, 28
.LBB0_76:
	s_or_b64 exec, exec, s[10:11]
	v_add_u32_e32 v10, s25, v19
	v_cmp_gt_i32_e64 s[12:13], s38, v10
	v_mov_b32_e32 v9, 0
	v_mov_b32_e32 v11, 0
	s_and_saveexec_b64 s[10:11], s[12:13]
	s_cbranch_execz .LBB0_78
	s_waitcnt vmcnt(59)
	v_ashrrev_i32_e32 v20, 6, v10
	v_readlane_b32 s16, v252, 21
	s_waitcnt vmcnt(58)
	v_ashrrev_i32_e32 v21, 31, v20
	v_readlane_b32 s20, v252, 25
	v_readlane_b32 s21, v252, 26
	v_readlane_b32 s17, v252, 22
	v_readlane_b32 s18, v252, 23
	v_lshl_add_u64 v[20:21], v[20:21], 2, s[20:21]
	global_load_dword v233, v[20:21], off
	v_readlane_b32 s19, v252, 24
	v_readlane_b32 s22, v252, 27
	v_readlane_b32 s23, v252, 28
.LBB0_78:
	s_or_b64 exec, exec, s[10:11]
	v_add_u32_e32 v8, s39, v19
	v_cmp_gt_i32_e64 s[10:11], s38, v8
	s_and_saveexec_b64 s[16:17], s[10:11]
	s_cbranch_execz .LBB0_80
	s_waitcnt vmcnt(59)
	v_ashrrev_i32_e32 v20, 6, v8
	v_readlane_b32 s56, v252, 21
	s_waitcnt vmcnt(58)
	v_ashrrev_i32_e32 v21, 31, v20
	v_readlane_b32 s60, v252, 25
	v_readlane_b32 s61, v252, 26
	v_readlane_b32 s57, v252, 22
	v_readlane_b32 s58, v252, 23
	v_lshl_add_u64 v[20:21], v[20:21], 2, s[60:61]
	global_load_dword v234, v[20:21], off
	v_readlane_b32 s59, v252, 24
	v_readlane_b32 s62, v252, 27
	v_readlane_b32 s63, v252, 28
.LBB0_80:
	s_or_b64 exec, exec, s[16:17]
	s_waitcnt vmcnt(0)
	v_cvt_f32_i32_e32 v6, v6
	v_cvt_f32_i32_e32 v12, v232
	v_cvt_f32_i32_e32 v11, v233
	v_cvt_f32_i32_e32 v9, v234
	v_mul_f32_e32 v13, v1, v6
	v_and_b32_e32 v20, 0x7fffffff, v13
	v_lshrrev_b32_e32 v6, 23, v20
	v_and_b32_e32 v21, 0x7fffff, v20
	v_cmp_nlt_f32_e64 s[22:23], |v13|, s41
	v_add_u32_e32 v22, 0xffffff88, v6
	v_or_b32_e32 v21, 0x800000, v21
	s_and_saveexec_b64 s[16:17], s[22:23]
	s_xor_b64 s[34:35], exec, s[16:17]
	s_cbranch_execz .LBB0_82
	v_cmp_lt_u32_e32 vcc, 63, v22
	v_mad_u64_u32 v[24:25], s[20:21], v21, s42, 0
	s_nop 0
	v_cndmask_b32_e32 v6, 0, v16, vcc
	v_add_u32_e32 v6, v6, v22
	v_cmp_lt_u32_e64 s[16:17], 31, v6
	s_nop 1
	v_cndmask_b32_e64 v23, 0, v17, s[16:17]
	v_add_u32_e32 v6, v23, v6
	v_cmp_lt_u32_e64 s[18:19], 31, v6
	s_nop 1
	v_cndmask_b32_e64 v23, 0, v17, s[18:19]
	v_add_u32_e32 v23, v23, v6
	v_mov_b32_e32 v6, v25
	v_mad_u64_u32 v[26:27], s[20:21], v21, s43, v[6:7]
	v_mov_b32_e32 v6, v27
	v_mad_u64_u32 v[28:29], s[20:21], v21, s44, v[6:7]
	v_mov_b32_e32 v6, v29
	v_mad_u64_u32 v[30:31], s[20:21], v21, s45, v[6:7]
	v_mov_b32_e32 v6, v31
	v_mad_u64_u32 v[32:33], s[20:21], v21, s46, v[6:7]
	v_mov_b32_e32 v6, v33
	v_mad_u64_u32 v[34:35], s[20:21], v21, s47, v[6:7]
	v_mov_b32_e32 v6, v35
	v_mad_u64_u32 v[36:37], s[20:21], v21, s48, v[6:7]
	v_cndmask_b32_e32 v25, v34, v30, vcc
	v_cndmask_b32_e32 v6, v36, v32, vcc
	v_cndmask_b32_e32 v29, v37, v34, vcc
	v_cndmask_b32_e64 v27, v6, v25, s[16:17]
	v_cndmask_b32_e64 v6, v29, v6, s[16:17]
	v_cndmask_b32_e32 v29, v32, v28, vcc
	v_cndmask_b32_e64 v25, v25, v29, s[16:17]
	v_sub_u32_e32 v31, 32, v23
	v_cmp_eq_u32_e64 s[20:21], 0, v23
	v_cndmask_b32_e32 v23, v30, v26, vcc
	v_cndmask_b32_e64 v6, v6, v27, s[18:19]
	v_cndmask_b32_e64 v27, v27, v25, s[18:19]
	v_cndmask_b32_e64 v26, v29, v23, s[16:17]
	v_alignbit_b32 v32, v6, v27, v31
	v_cndmask_b32_e64 v25, v25, v26, s[18:19]
	v_cndmask_b32_e64 v6, v32, v6, s[20:21]
	v_alignbit_b32 v29, v27, v25, v31
	v_cndmask_b32_e32 v24, v28, v24, vcc
	v_cndmask_b32_e64 v27, v29, v27, s[20:21]
	v_bfe_u32 v32, v6, 29, 1
	v_cndmask_b32_e64 v23, v23, v24, s[16:17]
	v_alignbit_b32 v29, v6, v27, 30
	v_sub_u32_e32 v33, 0, v32
	v_cndmask_b32_e64 v23, v26, v23, s[18:19]
	v_xor_b32_e32 v29, v29, v33
	v_alignbit_b32 v24, v25, v23, v31
	v_cndmask_b32_e64 v24, v24, v25, s[20:21]
	v_ffbh_u32_e32 v26, v29
	v_alignbit_b32 v25, v27, v24, 30
	v_min_u32_e32 v26, 32, v26
	v_alignbit_b32 v23, v24, v23, 30
	v_xor_b32_e32 v25, v25, v33
	v_sub_u32_e32 v27, 31, v26
	v_xor_b32_e32 v23, v23, v33
	v_alignbit_b32 v28, v29, v25, v27
	v_alignbit_b32 v23, v25, v23, v27
	v_alignbit_b32 v24, v28, v23, 9
	v_ffbh_u32_e32 v25, v24
	v_min_u32_e32 v25, 32, v25
	v_lshrrev_b32_e32 v30, 29, v6
	v_not_b32_e32 v27, v25
	v_alignbit_b32 v23, v24, v23, v27
	v_lshlrev_b32_e32 v24, 31, v30
	v_or_b32_e32 v27, 0x33000000, v24
	v_add_lshl_u32 v25, v25, v26, 23
	v_lshrrev_b32_e32 v23, 9, v23
	v_sub_u32_e32 v25, v27, v25
	v_or_b32_e32 v24, 0.5, v24
	v_lshlrev_b32_e32 v26, 23, v26
	v_or_b32_e32 v23, v25, v23
	v_lshrrev_b32_e32 v25, 9, v28
	v_sub_u32_e32 v24, v24, v26
	v_or_b32_e32 v24, v25, v24
	v_mul_f32_e32 v25, 0x3fc90fda, v24
	v_fma_f32 v26, v24, s49, -v25
	v_fmac_f32_e32 v26, 0x33a22168, v24
	v_fmac_f32_e32 v26, 0x3fc90fda, v23
	v_lshrrev_b32_e32 v6, 30, v6
	v_add_f32_e32 v24, v25, v26
	v_add_u32_e32 v23, v32, v6
